# attention: softmax VALU that sat behind the first two QK^T MFMAs hoisted in front of the segment's first LDS wait (fills the fragment-read latency bubble)
# baseline (speedup 1.0000x reference)
.LBB0_757:
	s_add_i32 s12, s64, -1
	s_sub_i32 s80, s11, 64
	s_cmp_lt_u32 s12, 3
	s_cselect_b32 s80, s10, s80
	s_mul_i32 s81, s80, 0xc00
	s_add_i32 s85, s82, 0x8000
	s_mov_b32 m0, s85
	s_add_i32 s85, s82, 0x10000
	buffer_load_dwordx4 v154, s[72:75], s81 offen lds
	s_mov_b32 m0, s85
	s_add_i32 s85, s82, 0xa000
	buffer_load_dwordx4 v155, s[72:75], s81 offen lds
	s_mov_b32 m0, s85
	s_add_i32 s81, s81, 0x18000
	buffer_load_dwordx4 v154, s[72:75], s81 offen lds
	s_lshl_b32 s81, s83, 11
	s_add_i32 s85, s82, 0x4000
	s_mov_b32 m0, s85
	s_add_i32 s85, s82, 0x6000
	buffer_load_dwordx4 v158, s[76:79], s81 offen lds
	s_mov_b32 m0, s85
	s_add_i32 s81, s81, 0x10000
	buffer_load_dwordx4 v158, s[76:79], s81 offen lds
	s_mov_b32 s84, s80
	s_add_i32 s6, 0, 0x12000
	v_add_u32_e32 v199, s6, v170
	v_add_u32_e32 v204, s6, v171
	v_add_u32_e32 v205, s6, v172
	ds_read_b128 v[64:67], v180 offset:49152
	ds_read_b128 v[68:71], v180 offset:57344
	ds_read_b128 v[200:203], v181 offset:49152
	ds_read_b128 v[226:229], v181 offset:57344
	ds_read_b128 v[230:233], v182 offset:49152
	ds_read_b128 v[234:237], v182 offset:57344
	ds_read_b128 v[238:241], v183 offset:49152
	ds_read_b128 v[242:245], v183 offset:57344
	v_exp_f32_e32 v216, v128
	v_add_f32_e32 v128, 0, v222
	v_add_f32_e32 v128, v224, v128
	v_add_f32_e32 v128, v220, v128
	v_add_f32_e32 v128, v223, v128
	v_add_f32_e32 v128, v219, v128
	v_add_f32_e32 v128, v221, v128
	v_add_f32_e32 v128, v217, v128
	v_add_f32_e32 v128, v218, v128
	v_add_f32_e32 v128, v212, v128
	v_add_f32_e32 v128, v214, v128
	v_add_f32_e32 v128, v211, v128
	v_add_f32_e32 v128, v213, v128
	v_exp_f32_e32 v138, v138
	s_waitcnt lgkmcnt(7)
	v_mfma_f32_32x32x16_bf16 v[80:95], v[64:67], v[124:127], 0
	s_waitcnt lgkmcnt(6)
	v_mfma_f32_32x32x16_bf16 v[64:79], v[68:71], v[124:127], 0
	s_waitcnt lgkmcnt(5)
	v_mfma_f32_32x32x16_bf16 v[80:95], v[200:203], v[120:123], v[80:95]
	v_add_f32_e32 v128, v208, v128
	v_exp_f32_e32 v139, v139
	v_add_f32_e32 v128, v210, v128
	v_exp_f32_e32 v164, v136
	v_add_f32_e32 v128, v207, v128
	v_exp_f32_e32 v137, v137
	v_add_f32_e32 v128, v209, v128
	s_waitcnt lgkmcnt(4)
	v_mfma_f32_32x32x16_bf16 v[64:79], v[226:229], v[120:123], v[64:79]
	ds_read_b128 v[200:203], v184 offset:49152
	ds_read_b128 v[226:229], v184 offset:57344
	v_exp_f32_e32 v165, v132
	v_add_f32_e32 v128, v138, v128
	v_add_f32_e32 v128, v139, v128
	v_exp_f32_e32 v206, v130
	v_add_f32_e32 v128, v164, v128
	v_exp_f32_e32 v215, v131
	s_waitcnt lgkmcnt(5)
	v_mfma_f32_32x32x16_bf16 v[80:95], v[230:233], v[116:119], v[80:95]
	v_add_f32_e32 v128, v137, v128
	v_add_f32_e32 v128, v165, v128
	v_exp_f32_e32 v225, v129
	v_exp_f32_e32 v162, v162
	v_exp_f32_e32 v163, v163
	v_exp_f32_e32 v160, v160
	v_exp_f32_e32 v161, v161
	s_waitcnt lgkmcnt(4)
	v_mfma_f32_32x32x16_bf16 v[64:79], v[234:237], v[116:119], v[64:79]
	ds_read_b128 v[230:233], v185 offset:49152
	ds_read_b128 v[234:237], v185 offset:57344
	v_cvt_pk_bf16_f32 v129, v220, v223
	v_cvt_pk_bf16_f32 v130, v219, v221
	v_cvt_pk_bf16_f32 v131, v217, v218
	v_cvt_pk_bf16_f32 v132, v212, v214
	v_cvt_pk_bf16_f32 v136, v138, v139
	v_cvt_pk_bf16_f32 v137, v164, v137
	s_waitcnt lgkmcnt(5)
	v_mfma_f32_32x32x16_bf16 v[80:95], v[238:241], v[112:115], v[80:95]
	v_cvt_pk_bf16_f32 v139, v206, v215
	v_permlane32_swap_b32_e32 v129, v131
	s_nop 0
	v_permlane32_swap_b32_e32 v137, v139
	s_waitcnt lgkmcnt(4)
	v_mfma_f32_32x32x16_bf16 v[64:79], v[242:245], v[112:115], v[64:79]
	ds_read_b128 v[238:241], v186 offset:49152
	ds_read_b128 v[242:245], v186 offset:57344
	s_waitcnt lgkmcnt(5)
	v_mfma_f32_32x32x16_bf16 v[80:95], v[200:203], v[108:111], v[80:95]
	s_waitcnt lgkmcnt(4)
	v_mfma_f32_32x32x16_bf16 v[64:79], v[226:229], v[108:111], v[64:79]
	ds_read_b128 v[200:203], v187 offset:49152
	ds_read_b128 v[226:229], v187 offset:57344
	s_waitcnt lgkmcnt(5)
	v_mfma_f32_32x32x16_bf16 v[80:95], v[230:233], v[104:107], v[80:95]
	s_waitcnt lgkmcnt(4)
	v_mfma_f32_32x32x16_bf16 v[64:79], v[234:237], v[104:107], v[64:79]
	ds_read_b128 v[230:233], v199
	ds_read_b128 v[234:237], v199 offset:4096
	ds_read_b128 v[246:249], v190
	s_waitcnt lgkmcnt(6)
	v_mfma_f32_32x32x16_bf16 v[80:95], v[238:241], v[100:103], v[80:95]
	s_waitcnt lgkmcnt(5)
	v_mfma_f32_32x32x16_bf16 v[64:79], v[242:245], v[100:103], v[64:79]
	ds_read_b128 v[238:241], v204
	ds_read_b128 v[242:245], v204 offset:4096
	ds_read_b128 v[250:253], v190 offset:1024
	v_add_u32_e32 v204, s6, v173
	s_waitcnt lgkmcnt(7)
	v_mfma_f32_32x32x16_bf16 v[80:95], v[200:203], v[96:99], v[80:95]
	s_waitcnt lgkmcnt(6)
	v_mfma_f32_32x32x16_bf16 v[64:79], v[226:229], v[96:99], v[64:79]
	ds_read_b128 v[200:203], v205
	ds_read_b128 v[226:229], v205 offset:4096
	s_waitcnt lgkmcnt(5)
	v_mfma_f32_32x32x16_bf16 v[80:95], v[230:233], v[246:249], v[80:95]
	s_waitcnt lgkmcnt(5)
	v_mfma_f32_32x32x16_bf16 v[64:79], v[234:237], v[246:249], v[64:79]
	ds_read_b128 v[230:233], v204
	ds_read_b128 v[234:237], v204 offset:4096
	ds_read_b128 v[246:249], v190 offset:2048
	s_waitcnt lgkmcnt(5)
	v_mfma_f32_32x32x16_bf16 v[80:95], v[238:241], v[250:253], v[80:95]
	s_waitcnt lgkmcnt(5)
	v_mfma_f32_32x32x16_bf16 v[64:79], v[242:245], v[250:253], v[64:79]
	ds_read_b128 v[250:253], v190 offset:3072
	s_waitcnt lgkmcnt(1)
	v_mfma_f32_32x32x16_bf16 v[80:95], v[200:203], v[246:249], v[80:95]
	v_exp_f32_e32 v205, v133
	v_cvt_pk_bf16_f32 v133, v211, v213
	v_cvt_pk_bf16_f32 v138, v165, v205
	v_add_f32_e32 v128, v205, v128
	v_add_f32_e32 v128, v206, v128
	v_add_f32_e32 v128, v215, v128
	s_waitcnt lgkmcnt(1)
	v_mfma_f32_32x32x16_bf16 v[64:79], v[226:229], v[246:249], v[64:79]
	v_add_f32_e32 v128, v216, v128
	v_add_f32_e32 v128, v225, v128
	v_add_f32_e32 v128, v162, v128
	v_add_f32_e32 v128, v163, v128
	v_add_f32_e32 v128, v160, v128
	v_add_f32_e32 v128, v161, v128
	s_waitcnt lgkmcnt(0)
	v_mfma_f32_32x32x16_bf16 v[80:95], v[230:233], v[250:253], v[80:95]
	v_exp_f32_e32 v226, v134
	v_exp_f32_e32 v227, v135
	v_cvt_pk_bf16_f32 v134, v208, v210
	v_cvt_pk_bf16_f32 v135, v207, v209
	v_add_f32_e32 v128, v226, v128
	v_add_f32_e32 v203, v227, v128
	v_mov_b32_e32 v204, v203
	s_waitcnt lgkmcnt(0)
	v_mfma_f32_32x32x16_bf16 v[64:79], v[234:237], v[250:253], v[64:79]
	s_nop 0
	v_permlane32_swap_b32_e32 v203, v204
	v_cvt_pk_bf16_f32 v128, v222, v224
	v_cvt_pk_bf16_f32 v208, v216, v225
	v_cvt_pk_bf16_f32 v209, v162, v163
	v_cvt_pk_bf16_f32 v210, v160, v161
	v_cvt_pk_bf16_f32 v211, v226, v227
	v_permlane32_swap_b32_e32 v132, v134
	v_permlane32_swap_b32_e32 v128, v130
	v_permlane32_swap_b32_e32 v133, v135
	v_permlane32_swap_b32_e32 v136, v138
	v_permlane32_swap_b32_e32 v208, v210
	v_permlane32_swap_b32_e32 v209, v211
	ds_read_b64_tr_b16 v[160:161], v167 offset:0
	ds_read_b64_tr_b16 v[162:163], v167 offset:0x800
	ds_read_b64_tr_b16 v[232:233], v167 offset:0x1000
	ds_read_b64_tr_b16 v[234:235], v167 offset:0x1800
	ds_read_b64_tr_b16 v[236:237], v167 offset:0x2000
	ds_read_b64_tr_b16 v[238:239], v167 offset:0x2800
	ds_read_b64_tr_b16 v[240:241], v167 offset:0x3000
	ds_read_b64_tr_b16 v[242:243], v167 offset:0x3800
	v_max_f32_e32 v164, v81, v81
	v_max_f32_e32 v165, v80, v80
	v_max_f32_e32 v164, v165, v164
	v_max3_f32 v164, v164, v82, v83
	v_max3_f32 v164, v164, v84, v85
	v_max3_f32 v164, v164, v86, v87
	v_max3_f32 v164, v164, v88, v89
	v_max3_f32 v164, v164, v90, v91
	v_max3_f32 v164, v164, v92, v93
	v_max3_f32 v164, v164, v94, v95
	s_waitcnt lgkmcnt(0)
	v_mfma_f32_32x32x16_bf16 v[16:31], v[128:131], v[160:163], v[16:31]
	v_max3_f32 v160, v164, v64, v65
	v_max3_f32 v160, v160, v66, v67
	v_max3_f32 v160, v160, v68, v69
	v_mfma_f32_32x32x16_bf16 v[16:31], v[132:135], v[232:235], v[16:31]
	ds_read_b64_tr_b16 v[232:233], v167 offset:0x200
	ds_read_b64_tr_b16 v[234:235], v167 offset:0xa00
	v_max3_f32 v160, v160, v70, v71
	v_max3_f32 v160, v160, v72, v73
	v_max3_f32 v160, v160, v74, v75
	v_mfma_f32_32x32x16_bf16 v[16:31], v[136:139], v[236:239], v[16:31]
	ds_read_b64_tr_b16 v[236:237], v167 offset:0x1200
	ds_read_b64_tr_b16 v[238:239], v167 offset:0x1a00
	ds_read_b64_tr_b16 v[244:245], v167 offset:0x2200
	ds_read_b64_tr_b16 v[246:247], v167 offset:0x2a00
	ds_read_b64_tr_b16 v[248:249], v167 offset:0x3200
	ds_read_b64_tr_b16 v[250:251], v167 offset:0x3a00
	v_max3_f32 v160, v160, v76, v77
	v_max3_f32 v160, v160, v78, v79
	v_mov_b32_e32 v161, v160
	v_mfma_f32_32x32x16_bf16 v[16:31], v[208:211], v[240:243], v[16:31]
	v_max_f32_e32 v162, v198, v198
	v_permlane32_swap_b32_e32 v160, v161
	v_max_f32_e32 v161, v161, v161
	v_max_f32_e32 v160, v160, v160
	v_max_f32_e32 v160, v160, v161
	s_waitcnt lgkmcnt(0)
	v_mfma_f32_32x32x16_bf16 v[32:47], v[128:131], v[232:235], v[32:47]
	ds_read_b64_tr_b16 v[232:233], v167 offset:0x400
	ds_read_b64_tr_b16 v[234:235], v167 offset:0xc00
	v_sub_f32_e32 v161, v160, v198
	v_max_f32_e32 v160, v162, v160
	v_sub_f32_e32 v162, v198, v160
	v_mul_f32_e32 v162, 0x3dd53b94, v162
	v_exp_f32_e32 v162, v162
	v_mfma_f32_32x32x16_bf16 v[32:47], v[132:135], v[236:239], v[32:47]
	ds_read_b64_tr_b16 v[236:237], v167 offset:0x1400
	ds_read_b64_tr_b16 v[238:239], v167 offset:0x1c00
	ds_read_b64_tr_b16 v[240:241], v167 offset:0x2400
	ds_read_b64_tr_b16 v[242:243], v167 offset:0x2c00
	v_cmp_ge_f32_e32 vcc, s48, v161
	s_cmp_eq_u64 vcc, exec
	s_cselect_b64 s[6:7], -1, 0
	v_cndmask_b32_e64 v206, v162, 1.0, s[6:7]
	v_cndmask_b32_e64 v160, v160, v198, s[6:7]
	v_mul_f32_e32 v205, 0xbdd53b94, v160
	v_cmp_gt_f32_e32 vcc, 1.0, v206
	v_mfma_f32_32x32x16_bf16 v[32:47], v[136:139], v[244:247], v[32:47]
	ds_read_b64_tr_b16 v[244:245], v167 offset:0x3400
	ds_read_b64_tr_b16 v[246:247], v167 offset:0x3c00
	v_fmamk_f32 v87, v87, 0x3dd53b94, v205
	v_fmamk_f32 v80, v80, 0x3dd53b94, v205
	v_fmamk_f32 v81, v81, 0x3dd53b94, v205
	v_fmamk_f32 v82, v82, 0x3dd53b94, v205
	v_fmamk_f32 v83, v83, 0x3dd53b94, v205
	v_mfma_f32_32x32x16_bf16 v[32:47], v[208:211], v[248:251], v[32:47]
	v_fmamk_f32 v84, v84, 0x3dd53b94, v205
	v_fmamk_f32 v85, v85, 0x3dd53b94, v205
	v_fmamk_f32 v86, v86, 0x3dd53b94, v205
	v_fmamk_f32 v88, v88, 0x3dd53b94, v205
	v_fmamk_f32 v89, v89, 0x3dd53b94, v205
	s_waitcnt lgkmcnt(0)
	v_mfma_f32_32x32x16_bf16 v[0:15], v[128:131], v[232:235], v[0:15]
	ds_read_b64_tr_b16 v[232:233], v167 offset:0x600
	ds_read_b64_tr_b16 v[234:235], v167 offset:0xe00
	v_fmamk_f32 v90, v90, 0x3dd53b94, v205
	v_fmamk_f32 v91, v91, 0x3dd53b94, v205
	v_fmamk_f32 v92, v92, 0x3dd53b94, v205
	v_fmamk_f32 v93, v93, 0x3dd53b94, v205
	v_fmamk_f32 v94, v94, 0x3dd53b94, v205
	v_mfma_f32_32x32x16_bf16 v[0:15], v[132:135], v[236:239], v[0:15]
	ds_read_b64_tr_b16 v[236:237], v167 offset:0x1600
	ds_read_b64_tr_b16 v[238:239], v167 offset:0x1e00
	v_fmamk_f32 v95, v95, 0x3dd53b94, v205
	v_fmamk_f32 v215, v64, 0x3dd53b94, v205
	v_fmamk_f32 v216, v65, 0x3dd53b94, v205
	v_fmamk_f32 v217, v66, 0x3dd53b94, v205
	v_fmamk_f32 v218, v67, 0x3dd53b94, v205
	v_mfma_f32_32x32x16_bf16 v[0:15], v[136:139], v[240:243], v[0:15]
	ds_read_b64_tr_b16 v[240:241], v167 offset:0x2600
	ds_read_b64_tr_b16 v[242:243], v167 offset:0x2e00
	ds_read_b64_tr_b16 v[248:249], v167 offset:0x3600
	ds_read_b64_tr_b16 v[250:251], v167 offset:0x3e00
	v_fmamk_f32 v219, v68, 0x3dd53b94, v205
	v_fmamk_f32 v212, v73, 0x3dd53b94, v205
	v_fmamk_f32 v213, v74, 0x3dd53b94, v205
	v_fmamk_f32 v214, v75, 0x3dd53b94, v205
	v_mfma_f32_32x32x16_bf16 v[0:15], v[208:211], v[244:247], v[0:15]
	v_fmamk_f32 v207, v76, 0x3dd53b94, v205
	v_fmamk_f32 v220, v77, 0x3dd53b94, v205
	v_fmamk_f32 v221, v78, 0x3dd53b94, v205
	s_waitcnt lgkmcnt(0)
	v_mfma_f32_32x32x16_bf16 v[48:63], v[128:131], v[232:235], v[48:63]
	v_exp_f32_e32 v128, v80
	v_exp_f32_e32 v129, v82
	v_exp_f32_e32 v130, v84
	v_exp_f32_e32 v131, v86
	v_mfma_f32_32x32x16_bf16 v[48:63], v[132:135], v[236:239], v[48:63]
	v_exp_f32_e32 v132, v88
	v_exp_f32_e32 v133, v90
	v_exp_f32_e32 v134, v92
	v_exp_f32_e32 v135, v94
	v_mfma_f32_32x32x16_bf16 v[48:63], v[136:139], v[240:243], v[48:63]
	v_exp_f32_e32 v139, v89
	v_exp_f32_e32 v138, v91
	v_exp_f32_e32 v137, v93
	v_exp_f32_e32 v136, v95
	v_mfma_f32_32x32x16_bf16 v[48:63], v[208:211], v[248:251], v[48:63]
	v_exp_f32_e32 v161, v87
	v_exp_f32_e32 v198, v81
	v_exp_f32_e32 v163, v83
	v_exp_f32_e32 v162, v85
	v_fmamk_f32 v208, v69, 0x3dd53b94, v205
	v_fmamk_f32 v209, v70, 0x3dd53b94, v205
	v_fmamk_f32 v210, v71, 0x3dd53b94, v205
	v_fmamk_f32 v211, v72, 0x3dd53b94, v205
	v_fmac_f32_e32 v205, 0x3dd53b94, v79
	s_cbranch_vccz .LBB0_761
	s_and_saveexec_b64 s[8:9], s[4:5]
	ds_write_b32 v189, v206 offset:128
	s_or_b64 exec, exec, s[8:9]
	s_waitcnt lgkmcnt(0)
	v_add_u32_e32 v248, s62, v169
	ds_read_b128 v[232:235], v248 offset:224
	ds_read_b128 v[236:239], v248 offset:192
	ds_read_b128 v[240:243], v248 offset:160
	ds_read_b128 v[244:247], v248 offset:128
	s_waitcnt lgkmcnt(3)
	v_pk_mul_f32 v[28:29], v[28:29], v[232:233]
	s_waitcnt lgkmcnt(2)
	v_pk_mul_f32 v[24:25], v[24:25], v[236:237]
	s_waitcnt lgkmcnt(1)
	v_pk_mul_f32 v[20:21], v[20:21], v[240:241]
	v_pk_mul_f32 v[30:31], v[30:31], v[234:235]
	v_pk_mul_f32 v[26:27], v[26:27], v[238:239]
	v_pk_mul_f32 v[22:23], v[22:23], v[242:243]
	s_waitcnt lgkmcnt(0)
	v_pk_mul_f32 v[18:19], v[18:19], v[246:247]
	v_pk_mul_f32 v[16:17], v[16:17], v[244:245]
	v_pk_mul_f32 v[44:45], v[44:45], v[232:233]
	v_pk_mul_f32 v[40:41], v[40:41], v[236:237]
	v_pk_mul_f32 v[36:37], v[36:37], v[240:241]
	v_pk_mul_f32 v[46:47], v[46:47], v[234:235]
	v_pk_mul_f32 v[42:43], v[42:43], v[238:239]
	v_pk_mul_f32 v[38:39], v[38:39], v[242:243]
	v_pk_mul_f32 v[34:35], v[34:35], v[246:247]
	v_pk_mul_f32 v[32:33], v[32:33], v[244:245]
	v_pk_mul_f32 v[12:13], v[12:13], v[232:233]
	v_pk_mul_f32 v[8:9], v[8:9], v[236:237]
	v_pk_mul_f32 v[4:5], v[4:5], v[240:241]
	v_pk_mul_f32 v[14:15], v[14:15], v[234:235]
	v_pk_mul_f32 v[10:11], v[10:11], v[238:239]
	v_pk_mul_f32 v[6:7], v[6:7], v[242:243]
	v_pk_mul_f32 v[2:3], v[2:3], v[246:247]
	v_pk_mul_f32 v[0:1], v[0:1], v[244:245]
	v_pk_mul_f32 v[60:61], v[60:61], v[232:233]
	v_pk_mul_f32 v[56:57], v[56:57], v[236:237]
	v_pk_mul_f32 v[52:53], v[52:53], v[240:241]
	v_pk_mul_f32 v[62:63], v[62:63], v[234:235]
	v_pk_mul_f32 v[58:59], v[58:59], v[238:239]
	v_pk_mul_f32 v[54:55], v[54:55], v[242:243]
	v_pk_mul_f32 v[50:51], v[50:51], v[246:247]
	v_pk_mul_f32 v[48:49], v[48:49], v[244:245]
.LBB0_761:
	s_waitcnt vmcnt(0) lgkmcnt(0)
	s_barrier
	s_add_i32 s80, s10, 64
	s_cmp_lt_u32 s12, 2
	s_cselect_b32 s80, s80, s11
	s_mul_i32 s81, s80, 0xc00
	s_add_i32 s85, s82, 0xc000
	s_mov_b32 m0, s85
	s_add_i32 s85, s82, 0x12000
	buffer_load_dwordx4 v154, s[72:75], s81 offen lds
	s_mov_b32 m0, s85
	s_add_i32 s85, s82, 0xe000
	buffer_load_dwordx4 v155, s[72:75], s81 offen lds
	s_mov_b32 m0, s85
	s_add_i32 s81, s81, 0x18000
	buffer_load_dwordx4 v154, s[72:75], s81 offen lds
	s_lshl_b32 s81, s84, 11
	s_add_i32 s85, s82, 0x0
	s_mov_b32 m0, s85
	s_add_i32 s85, s82, 0x2000
	buffer_load_dwordx4 v158, s[76:79], s81 offen lds
	s_mov_b32 m0, s85
	s_add_i32 s81, s81, 0x10000
	buffer_load_dwordx4 v158, s[76:79], s81 offen lds
	s_mov_b32 s83, s80
	ds_read_b128 v[64:67], v180 offset:32768
	ds_read_b128 v[68:71], v180 offset:40960
	ds_read_b128 v[222:225], v181 offset:32768
	ds_read_b128 v[226:229], v181 offset:40960
	ds_read_b128 v[230:233], v182 offset:32768
	ds_read_b128 v[234:237], v182 offset:40960
	ds_read_b128 v[238:241], v183 offset:32768
	ds_read_b128 v[242:245], v183 offset:40960
	v_exp_f32_e32 v164, v215
	v_add_f32_e32 v215, 0, v128
	v_add_f32_e32 v215, v198, v215
	v_add_f32_e32 v215, v129, v215
	v_add_f32_e32 v215, v163, v215
	v_add_f32_e32 v215, v130, v215
	v_add_f32_e32 v215, v162, v215
	v_add_f32_e32 v215, v131, v215
	v_add_f32_e32 v215, v161, v215
	v_add_f32_e32 v215, v132, v215
	v_add_f32_e32 v215, v139, v215
	v_add_f32_e32 v215, v133, v215
	v_add_f32_e32 v215, v138, v215
	v_add_f32_e32 v215, v134, v215
	v_exp_f32_e32 v165, v216
	v_add_f32_e32 v215, v137, v215
	s_waitcnt lgkmcnt(7)
	v_mfma_f32_32x32x16_bf16 v[80:95], v[64:67], v[124:127], 0
	s_waitcnt lgkmcnt(6)
	v_mfma_f32_32x32x16_bf16 v[64:79], v[68:71], v[124:127], 0
	s_waitcnt lgkmcnt(5)
	v_mfma_f32_32x32x16_bf16 v[80:95], v[222:225], v[120:123], v[80:95]
	v_exp_f32_e32 v217, v217
	v_add_f32_e32 v215, v135, v215
	v_exp_f32_e32 v218, v218
	v_add_f32_e32 v215, v136, v215
	v_exp_f32_e32 v219, v219
	v_add_f32_e32 v215, v164, v215
	v_exp_f32_e32 v208, v208
	s_waitcnt lgkmcnt(4)
	v_mfma_f32_32x32x16_bf16 v[64:79], v[226:229], v[120:123], v[64:79]
	ds_read_b128 v[222:225], v184 offset:32768
	ds_read_b128 v[226:229], v184 offset:40960
	v_add_f32_e32 v215, v165, v215
	v_exp_f32_e32 v209, v209
	v_add_f32_e32 v215, v217, v215
	v_exp_f32_e32 v210, v210
	v_add_f32_e32 v215, v218, v215
	v_exp_f32_e32 v211, v211
	s_waitcnt lgkmcnt(5)
	v_mfma_f32_32x32x16_bf16 v[80:95], v[230:233], v[116:119], v[80:95]
	v_add_f32_e32 v215, v219, v215
	v_exp_f32_e32 v212, v212
	v_add_f32_e32 v215, v208, v215
	v_exp_f32_e32 v213, v213
	v_add_f32_e32 v215, v209, v215
	v_exp_f32_e32 v214, v214
	v_add_f32_e32 v215, v210, v215
	s_waitcnt lgkmcnt(4)
	v_mfma_f32_32x32x16_bf16 v[64:79], v[234:237], v[116:119], v[64:79]
	ds_read_b128 v[230:233], v185 offset:32768
	ds_read_b128 v[234:237], v185 offset:40960
	v_exp_f32_e32 v207, v207
	v_add_f32_e32 v215, v211, v215
	v_exp_f32_e32 v220, v220
	v_add_f32_e32 v215, v212, v215
	v_exp_f32_e32 v221, v221
	v_add_f32_e32 v215, v213, v215
	s_waitcnt lgkmcnt(5)
	v_mfma_f32_32x32x16_bf16 v[80:95], v[238:241], v[112:115], v[80:95]
	v_exp_f32_e32 v205, v205
	v_add_f32_e32 v215, v214, v215
	v_add_f32_e32 v215, v207, v215
	v_add_f32_e32 v215, v220, v215
	v_add_f32_e32 v215, v221, v215
	v_add_f32_e32 v215, v205, v215
	v_mov_b32_e32 v216, v215
	s_waitcnt lgkmcnt(4)
	v_mfma_f32_32x32x16_bf16 v[64:79], v[242:245], v[112:115], v[64:79]
	ds_read_b128 v[238:241], v186 offset:32768
	ds_read_b128 v[242:245], v186 offset:40960
	v_permlane32_swap_b32_e32 v215, v216
	v_cvt_pk_bf16_f32 v128, v128, v198
	v_cvt_pk_bf16_f32 v129, v129, v163
	v_cvt_pk_bf16_f32 v130, v130, v162
	v_cvt_pk_bf16_f32 v131, v131, v161
	s_waitcnt lgkmcnt(5)
	v_mfma_f32_32x32x16_bf16 v[80:95], v[222:225], v[108:111], v[80:95]
	v_cvt_pk_bf16_f32 v132, v132, v139
	v_cvt_pk_bf16_f32 v133, v133, v138
	v_cvt_pk_bf16_f32 v134, v134, v137
	v_cvt_pk_bf16_f32 v135, v135, v136
	v_cvt_pk_bf16_f32 v136, v164, v165
	v_cvt_pk_bf16_f32 v137, v217, v218
	v_cvt_pk_bf16_f32 v138, v219, v208
	s_waitcnt lgkmcnt(4)
	v_mfma_f32_32x32x16_bf16 v[64:79], v[226:229], v[108:111], v[64:79]
	ds_read_b128 v[222:225], v187 offset:32768
	ds_read_b128 v[226:229], v187 offset:40960
	v_cvt_pk_bf16_f32 v139, v209, v210
	v_cvt_pk_bf16_f32 v208, v211, v212
	v_cvt_pk_bf16_f32 v209, v213, v214
	v_cvt_pk_bf16_f32 v210, v207, v220
	v_cvt_pk_bf16_f32 v211, v221, v205
	v_permlane32_swap_b32_e32 v128, v130
	s_waitcnt lgkmcnt(5)
	v_mfma_f32_32x32x16_bf16 v[80:95], v[230:233], v[104:107], v[80:95]
	v_permlane32_swap_b32_e32 v129, v131
	v_permlane32_swap_b32_e32 v132, v134
	v_permlane32_swap_b32_e32 v133, v135
	v_permlane32_swap_b32_e32 v136, v138
	s_waitcnt lgkmcnt(4)
	v_mfma_f32_32x32x16_bf16 v[64:79], v[234:237], v[104:107], v[64:79]
	ds_read_b128 v[230:233], v191
	ds_read_b128 v[234:237], v191 offset:4096
	ds_read_b128 v[246:249], v190
	v_permlane32_swap_b32_e32 v137, v139
	v_permlane32_swap_b32_e32 v208, v210
	v_permlane32_swap_b32_e32 v209, v211
	s_waitcnt lgkmcnt(6)
	v_mfma_f32_32x32x16_bf16 v[80:95], v[238:241], v[100:103], v[80:95]
	s_waitcnt lgkmcnt(5)
	v_mfma_f32_32x32x16_bf16 v[64:79], v[242:245], v[100:103], v[64:79]
	ds_read_b128 v[238:241], v192
	ds_read_b128 v[242:245], v192 offset:4096
	ds_read_b128 v[250:253], v190 offset:1024
	s_waitcnt lgkmcnt(7)
	v_mfma_f32_32x32x16_bf16 v[80:95], v[222:225], v[96:99], v[80:95]
	s_waitcnt lgkmcnt(6)
	v_mfma_f32_32x32x16_bf16 v[64:79], v[226:229], v[96:99], v[64:79]
	ds_read_b128 v[222:225], v193
	ds_read_b128 v[226:229], v193 offset:4096
	s_waitcnt lgkmcnt(5)
	v_mfma_f32_32x32x16_bf16 v[80:95], v[230:233], v[246:249], v[80:95]
	s_waitcnt lgkmcnt(5)
	v_mfma_f32_32x32x16_bf16 v[64:79], v[234:237], v[246:249], v[64:79]
	ds_read_b128 v[230:233], v194
	ds_read_b128 v[234:237], v194 offset:4096
	ds_read_b128 v[246:249], v190 offset:2048
	s_waitcnt lgkmcnt(5)
	v_mfma_f32_32x32x16_bf16 v[80:95], v[238:241], v[250:253], v[80:95]
	s_waitcnt lgkmcnt(5)
	v_mfma_f32_32x32x16_bf16 v[64:79], v[242:245], v[250:253], v[64:79]
	ds_read_b128 v[250:253], v190 offset:3072
	s_waitcnt lgkmcnt(1)
	v_mfma_f32_32x32x16_bf16 v[80:95], v[222:225], v[246:249], v[80:95]
	s_waitcnt lgkmcnt(1)
	v_mfma_f32_32x32x16_bf16 v[64:79], v[226:229], v[246:249], v[64:79]
	s_waitcnt lgkmcnt(0)
	v_mfma_f32_32x32x16_bf16 v[80:95], v[230:233], v[250:253], v[80:95]
	s_waitcnt lgkmcnt(0)
	v_mfma_f32_32x32x16_bf16 v[64:79], v[234:237], v[250:253], v[64:79]
	ds_read_b64_tr_b16 v[238:239], v174 offset:0
	ds_read_b64_tr_b16 v[240:241], v174 offset:0x800
	ds_read_b64_tr_b16 v[242:243], v174 offset:0x1000
	ds_read_b64_tr_b16 v[244:245], v174 offset:0x1800
	ds_read_b64_tr_b16 v[246:247], v174 offset:0x2000
	ds_read_b64_tr_b16 v[248:249], v174 offset:0x2800
	ds_read_b64_tr_b16 v[250:251], v174 offset:0x3000
	ds_read_b64_tr_b16 v[252:253], v174 offset:0x3800
	s_nop 3
	v_max_f32_e32 v161, v81, v81
	v_max_f32_e32 v162, v80, v80
	v_max_f32_e32 v161, v162, v161
	v_max3_f32 v161, v161, v82, v83
	v_max3_f32 v161, v161, v84, v85
	v_max3_f32 v161, v161, v86, v87
	v_max3_f32 v161, v161, v88, v89
	v_max3_f32 v161, v161, v90, v91
	v_max3_f32 v161, v161, v92, v93
	v_max3_f32 v161, v161, v94, v95
	s_waitcnt lgkmcnt(0)
	v_mfma_f32_32x32x16_bf16 v[16:31], v[128:131], v[238:241], v[16:31]
	ds_read_b64_tr_b16 v[238:239], v174 offset:0x200
	ds_read_b64_tr_b16 v[240:241], v174 offset:0xa00
	v_max3_f32 v161, v161, v64, v65
	v_max3_f32 v161, v161, v66, v67
	v_max3_f32 v161, v161, v68, v69
	v_mfma_f32_32x32x16_bf16 v[16:31], v[132:135], v[242:245], v[16:31]
	ds_read_b64_tr_b16 v[242:243], v174 offset:0x1200
	ds_read_b64_tr_b16 v[244:245], v174 offset:0x1a00
	v_max3_f32 v161, v161, v70, v71
	v_max3_f32 v161, v161, v72, v73
	v_max3_f32 v161, v161, v74, v75
	v_mfma_f32_32x32x16_bf16 v[16:31], v[136:139], v[246:249], v[16:31]
	ds_read_b64_tr_b16 v[246:247], v174 offset:0x2200
	ds_read_b64_tr_b16 v[248:249], v174 offset:0x2a00
	ds_read_b64_tr_b16 v[162:163], v174 offset:0x3200
	ds_read_b64_tr_b16 v[164:165], v174 offset:0x3a00
	v_max3_f32 v161, v161, v76, v77
	v_max3_f32 v161, v161, v78, v79
	v_mov_b32_e32 v198, v161
	v_mfma_f32_32x32x16_bf16 v[16:31], v[208:211], v[250:253], v[16:31]
	v_max_f32_e32 v205, v160, v160
	v_permlane32_swap_b32_e32 v161, v198
	v_max_f32_e32 v198, v198, v198
	v_max_f32_e32 v161, v161, v161
	v_max_f32_e32 v161, v161, v198
	s_waitcnt lgkmcnt(0)
	v_mfma_f32_32x32x16_bf16 v[32:47], v[128:131], v[238:241], v[32:47]
	ds_read_b64_tr_b16 v[238:239], v174 offset:0x400
	ds_read_b64_tr_b16 v[240:241], v174 offset:0xc00
	v_sub_f32_e32 v198, v161, v160
	v_max_f32_e32 v161, v205, v161
	v_sub_f32_e32 v205, v160, v161
	v_mul_f32_e32 v205, 0x3dd53b94, v205
	v_exp_f32_e32 v205, v205
	v_mfma_f32_32x32x16_bf16 v[32:47], v[132:135], v[242:245], v[32:47]
	ds_read_b64_tr_b16 v[242:243], v174 offset:0x1400
	ds_read_b64_tr_b16 v[244:245], v174 offset:0x1c00
	v_cmp_ge_f32_e32 vcc, s48, v198
	s_cmp_eq_u64 vcc, exec
	s_cselect_b64 s[6:7], -1, 0
	v_cndmask_b32_e64 v205, v205, 1.0, s[6:7]
	v_cndmask_b32_e64 v198, v161, v160, s[6:7]
	v_mul_f32_e32 v236, 0xbdd53b94, v198
	v_mov_b32_e32 v237, v236
	v_cmp_gt_f32_e32 vcc, 1.0, v205
	v_mfma_f32_32x32x16_bf16 v[32:47], v[136:139], v[246:249], v[32:47]
	ds_read_b64_tr_b16 v[246:247], v174 offset:0x2400
	ds_read_b64_tr_b16 v[248:249], v174 offset:0x2c00
	ds_read_b64_tr_b16 v[250:251], v174 offset:0x3400
	ds_read_b64_tr_b16 v[252:253], v174 offset:0x3c00
	v_fmamk_f32 v80, v80, 0x3dd53b94, v236
	v_fmamk_f32 v81, v81, 0x3dd53b94, v236
	v_fmamk_f32 v82, v82, 0x3dd53b94, v236
	v_fmamk_f32 v83, v83, 0x3dd53b94, v236
	v_mfma_f32_32x32x16_bf16 v[32:47], v[208:211], v[162:165], v[32:47]
	v_fmamk_f32 v84, v84, 0x3dd53b94, v236
	v_fmamk_f32 v85, v85, 0x3dd53b94, v236
	v_fmamk_f32 v86, v86, 0x3dd53b94, v236
	v_fmamk_f32 v87, v87, 0x3dd53b94, v236
	s_waitcnt lgkmcnt(0)
	v_mfma_f32_32x32x16_bf16 v[0:15], v[128:131], v[238:241], v[0:15]
	ds_read_b64_tr_b16 v[162:163], v174 offset:0x600
	ds_read_b64_tr_b16 v[164:165], v174 offset:0xe00
	ds_read_b64_tr_b16 v[238:239], v174 offset:0x1600
	ds_read_b64_tr_b16 v[240:241], v174 offset:0x1e00
	v_fmamk_f32 v88, v88, 0x3dd53b94, v236
	v_fmamk_f32 v89, v89, 0x3dd53b94, v236
	v_fmamk_f32 v90, v90, 0x3dd53b94, v236
	v_fmamk_f32 v91, v91, 0x3dd53b94, v236
	v_mfma_f32_32x32x16_bf16 v[0:15], v[132:135], v[242:245], v[0:15]
	ds_read_b64_tr_b16 v[242:243], v174 offset:0x2600
	ds_read_b64_tr_b16 v[244:245], v174 offset:0x2e00
	v_fmamk_f32 v92, v92, 0x3dd53b94, v236
	v_fmamk_f32 v93, v93, 0x3dd53b94, v236
	v_fmamk_f32 v94, v94, 0x3dd53b94, v236
	v_fmamk_f32 v95, v95, 0x3dd53b94, v236
	v_mfma_f32_32x32x16_bf16 v[0:15], v[136:139], v[246:249], v[0:15]
	ds_read_b64_tr_b16 v[246:247], v174 offset:0x3600
	ds_read_b64_tr_b16 v[248:249], v174 offset:0x3e00
	v_exp_f32_e32 v222, v80
	v_exp_f32_e32 v224, v81
	v_exp_f32_e32 v220, v82
	v_mfma_f32_32x32x16_bf16 v[0:15], v[208:211], v[250:253], v[0:15]
	v_exp_f32_e32 v223, v83
	v_exp_f32_e32 v219, v84
	v_exp_f32_e32 v221, v85
	s_waitcnt lgkmcnt(0)
	v_mfma_f32_32x32x16_bf16 v[48:63], v[128:131], v[162:165], v[48:63]
	v_exp_f32_e32 v217, v86
	v_exp_f32_e32 v218, v87
	v_exp_f32_e32 v212, v88
	v_pk_fma_f32 v[130:131], v[70:71], s[28:29], v[236:237] op_sel_hi:[1,0,0]
	v_pk_fma_f32 v[128:129], v[72:73], s[28:29], v[236:237] op_sel_hi:[1,0,0]
	v_mfma_f32_32x32x16_bf16 v[48:63], v[132:135], v[238:241], v[48:63]
	v_exp_f32_e32 v214, v89
	v_exp_f32_e32 v213, v91
	v_exp_f32_e32 v207, v94
	v_pk_fma_f32 v[132:133], v[68:69], s[28:29], v[236:237] op_sel_hi:[1,0,0]
	v_pk_fma_f32 v[134:135], v[78:79], s[28:29], v[236:237] op_sel_hi:[1,0,0]
	v_mfma_f32_32x32x16_bf16 v[48:63], v[136:139], v[242:245], v[48:63]
	v_pk_fma_f32 v[138:139], v[64:65], s[28:29], v[236:237] op_sel_hi:[1,0,0]
	v_pk_fma_f32 v[136:137], v[66:67], s[28:29], v[236:237] op_sel_hi:[1,0,0]
	v_pk_fma_f32 v[162:163], v[74:75], s[28:29], v[236:237] op_sel_hi:[1,0,0]
	v_pk_fma_f32 v[160:161], v[76:77], s[28:29], v[236:237] op_sel_hi:[1,0,0]
	v_mfma_f32_32x32x16_bf16 v[48:63], v[208:211], v[246:249], v[48:63]
	v_exp_f32_e32 v211, v90
	v_exp_f32_e32 v208, v92
	v_exp_f32_e32 v210, v93
	v_exp_f32_e32 v209, v95
	v_add_f32_e32 v64, v203, v204
	v_fmac_f32_e32 v64, v197, v140
	v_add_f32_e32 v140, v215, v216
	s_addk_i32 s10, 0x80
	s_add_i32 s64, s64, 2
	s_addk_i32 s11, 0x80
	v_fmac_f32_e32 v140, v64, v206
	s_cbranch_vccz .LBB0_765
	s_and_saveexec_b64 s[8:9], s[4:5]
	ds_write_b32 v189, v205 offset:128
	s_or_b64 exec, exec, s[8:9]
	s_waitcnt lgkmcnt(0)
	v_add_u32_e32 v164, s62, v169
	ds_read_b128 v[238:241], v164 offset:224
	ds_read_b128 v[242:245], v164 offset:192
	ds_read_b128 v[246:249], v164 offset:160
	ds_read_b128 v[250:253], v164 offset:128
	s_waitcnt lgkmcnt(3)
	v_pk_mul_f32 v[28:29], v[28:29], v[238:239]
	s_waitcnt lgkmcnt(2)
	v_pk_mul_f32 v[24:25], v[24:25], v[242:243]
	s_waitcnt lgkmcnt(1)
	v_pk_mul_f32 v[20:21], v[20:21], v[246:247]
	v_pk_mul_f32 v[30:31], v[30:31], v[240:241]
	v_pk_mul_f32 v[26:27], v[26:27], v[244:245]
	v_pk_mul_f32 v[22:23], v[22:23], v[248:249]
	s_waitcnt lgkmcnt(0)
	v_pk_mul_f32 v[18:19], v[18:19], v[252:253]
	v_pk_mul_f32 v[16:17], v[16:17], v[250:251]
	v_pk_mul_f32 v[44:45], v[44:45], v[238:239]
	v_pk_mul_f32 v[40:41], v[40:41], v[242:243]
	v_pk_mul_f32 v[36:37], v[36:37], v[246:247]
	v_pk_mul_f32 v[46:47], v[46:47], v[240:241]
	v_pk_mul_f32 v[42:43], v[42:43], v[244:245]
	v_pk_mul_f32 v[38:39], v[38:39], v[248:249]
	v_pk_mul_f32 v[34:35], v[34:35], v[252:253]
	v_pk_mul_f32 v[32:33], v[32:33], v[250:251]
	v_pk_mul_f32 v[12:13], v[12:13], v[238:239]
	v_pk_mul_f32 v[8:9], v[8:9], v[242:243]
	v_pk_mul_f32 v[4:5], v[4:5], v[246:247]
	v_pk_mul_f32 v[14:15], v[14:15], v[240:241]
	v_pk_mul_f32 v[10:11], v[10:11], v[244:245]
	v_pk_mul_f32 v[6:7], v[6:7], v[248:249]
	v_pk_mul_f32 v[2:3], v[2:3], v[252:253]
	v_pk_mul_f32 v[0:1], v[0:1], v[250:251]
	v_pk_mul_f32 v[60:61], v[60:61], v[238:239]
	v_pk_mul_f32 v[56:57], v[56:57], v[242:243]
	v_pk_mul_f32 v[52:53], v[52:53], v[246:247]
	v_pk_mul_f32 v[62:63], v[62:63], v[240:241]
	v_pk_mul_f32 v[58:59], v[58:59], v[244:245]
	v_pk_mul_f32 v[54:55], v[54:55], v[248:249]
	v_pk_mul_f32 v[50:51], v[50:51], v[252:253]
	v_pk_mul_f32 v[48:49], v[48:49], v[250:251]

.LBB0_2012:
	s_add_i32 s8, s8, 2
	s_sub_i32 s80, s14, 64
	s_cmp_lt_u32 s8, 3
	s_cselect_b32 s80, s13, s80
	s_mul_i32 s81, s80, 0xc00
	s_add_i32 s85, s82, 0x8000
	s_mov_b32 m0, s85
	s_add_i32 s85, s82, 0x10000
	buffer_load_dwordx4 v154, s[72:75], s81 offen lds
	s_mov_b32 m0, s85
	s_add_i32 s85, s82, 0xa000
	buffer_load_dwordx4 v155, s[72:75], s81 offen lds
	s_mov_b32 m0, s85
	s_add_i32 s81, s81, 0x18000
	buffer_load_dwordx4 v154, s[72:75], s81 offen lds
	s_lshl_b32 s81, s83, 11
	s_add_i32 s85, s82, 0x4000
	s_mov_b32 m0, s85
	s_add_i32 s85, s82, 0x6000
	buffer_load_dwordx4 v158, s[76:79], s81 offen lds
	s_mov_b32 m0, s85
	s_add_i32 s81, s81, 0x10000
	buffer_load_dwordx4 v158, s[76:79], s81 offen lds
	s_mov_b32 s84, s80
	s_add_i32 s6, 0, 0x12000
	v_add_u32_e32 v199, s6, v170
	v_add_u32_e32 v204, s6, v171
	v_add_u32_e32 v205, s6, v172
	ds_read_b128 v[64:67], v180 offset:49152
	ds_read_b128 v[68:71], v180 offset:57344
	ds_read_b128 v[200:203], v181 offset:49152
	ds_read_b128 v[226:229], v181 offset:57344
	ds_read_b128 v[230:233], v182 offset:49152
	ds_read_b128 v[234:237], v182 offset:57344
	ds_read_b128 v[238:241], v183 offset:49152
	ds_read_b128 v[242:245], v183 offset:57344
	v_exp_f32_e32 v216, v128
	v_add_f32_e32 v128, 0, v222
	v_add_f32_e32 v128, v224, v128
	v_add_f32_e32 v128, v220, v128
	v_add_f32_e32 v128, v223, v128
	v_add_f32_e32 v128, v219, v128
	v_add_f32_e32 v128, v221, v128
	v_add_f32_e32 v128, v217, v128
	v_add_f32_e32 v128, v218, v128
	v_add_f32_e32 v128, v212, v128
	v_add_f32_e32 v128, v214, v128
	v_add_f32_e32 v128, v211, v128
	v_add_f32_e32 v128, v213, v128
	v_exp_f32_e32 v138, v138
	s_waitcnt lgkmcnt(7)
	v_mfma_f32_32x32x16_bf16 v[80:95], v[64:67], v[124:127], 0
	s_waitcnt lgkmcnt(6)
	v_mfma_f32_32x32x16_bf16 v[64:79], v[68:71], v[124:127], 0
	s_waitcnt lgkmcnt(5)
	v_mfma_f32_32x32x16_bf16 v[80:95], v[200:203], v[120:123], v[80:95]
	v_add_f32_e32 v128, v208, v128
	v_exp_f32_e32 v139, v139
	v_add_f32_e32 v128, v210, v128
	v_exp_f32_e32 v164, v136
	v_add_f32_e32 v128, v207, v128
	v_exp_f32_e32 v137, v137
	v_add_f32_e32 v128, v209, v128
	s_waitcnt lgkmcnt(4)
	v_mfma_f32_32x32x16_bf16 v[64:79], v[226:229], v[120:123], v[64:79]
	ds_read_b128 v[200:203], v184 offset:49152
	ds_read_b128 v[226:229], v184 offset:57344
	v_exp_f32_e32 v165, v132
	v_add_f32_e32 v128, v138, v128
	v_add_f32_e32 v128, v139, v128
	v_exp_f32_e32 v206, v130
	v_add_f32_e32 v128, v164, v128
	v_exp_f32_e32 v215, v131
	s_waitcnt lgkmcnt(5)
	v_mfma_f32_32x32x16_bf16 v[80:95], v[230:233], v[116:119], v[80:95]
	v_add_f32_e32 v128, v137, v128
	v_add_f32_e32 v128, v165, v128
	v_exp_f32_e32 v225, v129
	v_exp_f32_e32 v162, v162
	v_exp_f32_e32 v163, v163
	v_exp_f32_e32 v160, v160
	v_exp_f32_e32 v161, v161
	s_waitcnt lgkmcnt(4)
	v_mfma_f32_32x32x16_bf16 v[64:79], v[234:237], v[116:119], v[64:79]
	ds_read_b128 v[230:233], v185 offset:49152
	ds_read_b128 v[234:237], v185 offset:57344
	v_cvt_pk_bf16_f32 v129, v220, v223
	v_cvt_pk_bf16_f32 v130, v219, v221
	v_cvt_pk_bf16_f32 v131, v217, v218
	v_cvt_pk_bf16_f32 v132, v212, v214
	v_cvt_pk_bf16_f32 v136, v138, v139
	v_cvt_pk_bf16_f32 v137, v164, v137
	s_waitcnt lgkmcnt(5)
	v_mfma_f32_32x32x16_bf16 v[80:95], v[238:241], v[112:115], v[80:95]
	v_cvt_pk_bf16_f32 v139, v206, v215
	v_permlane32_swap_b32_e32 v129, v131
	s_nop 0
	v_permlane32_swap_b32_e32 v137, v139
	s_waitcnt lgkmcnt(4)
	v_mfma_f32_32x32x16_bf16 v[64:79], v[242:245], v[112:115], v[64:79]
	ds_read_b128 v[238:241], v186 offset:49152
	ds_read_b128 v[242:245], v186 offset:57344
	s_waitcnt lgkmcnt(5)
	v_mfma_f32_32x32x16_bf16 v[80:95], v[200:203], v[108:111], v[80:95]
	s_waitcnt lgkmcnt(4)
	v_mfma_f32_32x32x16_bf16 v[64:79], v[226:229], v[108:111], v[64:79]
	ds_read_b128 v[200:203], v187 offset:49152
	ds_read_b128 v[226:229], v187 offset:57344
	s_waitcnt lgkmcnt(5)
	v_mfma_f32_32x32x16_bf16 v[80:95], v[230:233], v[104:107], v[80:95]
	s_waitcnt lgkmcnt(4)
	v_mfma_f32_32x32x16_bf16 v[64:79], v[234:237], v[104:107], v[64:79]
	ds_read_b128 v[230:233], v199
	ds_read_b128 v[234:237], v199 offset:4096
	ds_read_b128 v[246:249], v190
	s_waitcnt lgkmcnt(6)
	v_mfma_f32_32x32x16_bf16 v[80:95], v[238:241], v[100:103], v[80:95]
	s_waitcnt lgkmcnt(5)
	v_mfma_f32_32x32x16_bf16 v[64:79], v[242:245], v[100:103], v[64:79]
	ds_read_b128 v[238:241], v204
	ds_read_b128 v[242:245], v204 offset:4096
	ds_read_b128 v[250:253], v190 offset:1024
	v_add_u32_e32 v204, s6, v173
	s_waitcnt lgkmcnt(7)
	v_mfma_f32_32x32x16_bf16 v[80:95], v[200:203], v[96:99], v[80:95]
	s_waitcnt lgkmcnt(6)
	v_mfma_f32_32x32x16_bf16 v[64:79], v[226:229], v[96:99], v[64:79]
	ds_read_b128 v[200:203], v205
	ds_read_b128 v[226:229], v205 offset:4096
	s_waitcnt lgkmcnt(5)
	v_mfma_f32_32x32x16_bf16 v[80:95], v[230:233], v[246:249], v[80:95]
	s_waitcnt lgkmcnt(5)
	v_mfma_f32_32x32x16_bf16 v[64:79], v[234:237], v[246:249], v[64:79]
	ds_read_b128 v[230:233], v204
	ds_read_b128 v[234:237], v204 offset:4096
	ds_read_b128 v[246:249], v190 offset:2048
	s_waitcnt lgkmcnt(5)
	v_mfma_f32_32x32x16_bf16 v[80:95], v[238:241], v[250:253], v[80:95]
	s_waitcnt lgkmcnt(5)
	v_mfma_f32_32x32x16_bf16 v[64:79], v[242:245], v[250:253], v[64:79]
	ds_read_b128 v[250:253], v190 offset:3072
	s_waitcnt lgkmcnt(1)
	v_mfma_f32_32x32x16_bf16 v[80:95], v[200:203], v[246:249], v[80:95]
	v_exp_f32_e32 v205, v133
	v_cvt_pk_bf16_f32 v133, v211, v213
	v_cvt_pk_bf16_f32 v138, v165, v205
	v_add_f32_e32 v128, v205, v128
	v_add_f32_e32 v128, v206, v128
	v_add_f32_e32 v128, v215, v128
	s_waitcnt lgkmcnt(1)
	v_mfma_f32_32x32x16_bf16 v[64:79], v[226:229], v[246:249], v[64:79]
	v_add_f32_e32 v128, v216, v128
	v_add_f32_e32 v128, v225, v128
	v_add_f32_e32 v128, v162, v128
	v_add_f32_e32 v128, v163, v128
	v_add_f32_e32 v128, v160, v128
	v_add_f32_e32 v128, v161, v128
	s_waitcnt lgkmcnt(0)
	v_mfma_f32_32x32x16_bf16 v[80:95], v[230:233], v[250:253], v[80:95]
	v_exp_f32_e32 v226, v134
	v_exp_f32_e32 v227, v135
	v_cvt_pk_bf16_f32 v134, v208, v210
	v_cvt_pk_bf16_f32 v135, v207, v209
	v_add_f32_e32 v128, v226, v128
	v_add_f32_e32 v203, v227, v128
	v_mov_b32_e32 v204, v203
	s_waitcnt lgkmcnt(0)
	v_mfma_f32_32x32x16_bf16 v[64:79], v[234:237], v[250:253], v[64:79]
	s_nop 0
	v_permlane32_swap_b32_e32 v203, v204
	v_cvt_pk_bf16_f32 v128, v222, v224
	v_cvt_pk_bf16_f32 v208, v216, v225
	v_cvt_pk_bf16_f32 v209, v162, v163
	v_cvt_pk_bf16_f32 v210, v160, v161
	v_cvt_pk_bf16_f32 v211, v226, v227
	v_permlane32_swap_b32_e32 v132, v134
	v_permlane32_swap_b32_e32 v128, v130
	v_permlane32_swap_b32_e32 v133, v135
	v_permlane32_swap_b32_e32 v136, v138
	v_permlane32_swap_b32_e32 v208, v210
	v_permlane32_swap_b32_e32 v209, v211
	ds_read_b64_tr_b16 v[160:161], v167 offset:0
	ds_read_b64_tr_b16 v[162:163], v167 offset:0x800
	ds_read_b64_tr_b16 v[232:233], v167 offset:0x1000
	ds_read_b64_tr_b16 v[234:235], v167 offset:0x1800
	ds_read_b64_tr_b16 v[236:237], v167 offset:0x2000
	ds_read_b64_tr_b16 v[238:239], v167 offset:0x2800
	ds_read_b64_tr_b16 v[240:241], v167 offset:0x3000
	ds_read_b64_tr_b16 v[242:243], v167 offset:0x3800
	v_max_f32_e32 v164, v81, v81
	v_max_f32_e32 v165, v80, v80
	v_max_f32_e32 v164, v165, v164
	v_max3_f32 v164, v164, v82, v83
	v_max3_f32 v164, v164, v84, v85
	v_max3_f32 v164, v164, v86, v87
	v_max3_f32 v164, v164, v88, v89
	v_max3_f32 v164, v164, v90, v91
	v_max3_f32 v164, v164, v92, v93
	v_max3_f32 v164, v164, v94, v95
	s_waitcnt lgkmcnt(0)
	v_mfma_f32_32x32x16_bf16 v[0:15], v[128:131], v[160:163], v[0:15]
	v_max3_f32 v160, v164, v64, v65
	v_max3_f32 v160, v160, v66, v67
	v_max3_f32 v160, v160, v68, v69
	v_mfma_f32_32x32x16_bf16 v[0:15], v[132:135], v[232:235], v[0:15]
	ds_read_b64_tr_b16 v[232:233], v167 offset:0x200
	ds_read_b64_tr_b16 v[234:235], v167 offset:0xa00
	v_max3_f32 v160, v160, v70, v71
	v_max3_f32 v160, v160, v72, v73
	v_max3_f32 v160, v160, v74, v75
	v_mfma_f32_32x32x16_bf16 v[0:15], v[136:139], v[236:239], v[0:15]
	ds_read_b64_tr_b16 v[236:237], v167 offset:0x1200
	ds_read_b64_tr_b16 v[238:239], v167 offset:0x1a00
	ds_read_b64_tr_b16 v[244:245], v167 offset:0x2200
	ds_read_b64_tr_b16 v[246:247], v167 offset:0x2a00
	ds_read_b64_tr_b16 v[248:249], v167 offset:0x3200
	ds_read_b64_tr_b16 v[250:251], v167 offset:0x3a00
	v_max3_f32 v160, v160, v76, v77
	v_max3_f32 v160, v160, v78, v79
	v_mov_b32_e32 v161, v160
	v_mfma_f32_32x32x16_bf16 v[0:15], v[208:211], v[240:243], v[0:15]
	v_max_f32_e32 v162, v198, v198
	v_permlane32_swap_b32_e32 v160, v161
	v_max_f32_e32 v161, v161, v161
	v_max_f32_e32 v160, v160, v160
	v_max_f32_e32 v160, v160, v161
	s_waitcnt lgkmcnt(0)
	v_mfma_f32_32x32x16_bf16 v[32:47], v[128:131], v[232:235], v[32:47]
	ds_read_b64_tr_b16 v[232:233], v167 offset:0x400
	ds_read_b64_tr_b16 v[234:235], v167 offset:0xc00
	v_sub_f32_e32 v161, v160, v198
	v_max_f32_e32 v160, v162, v160
	v_sub_f32_e32 v162, v198, v160
	v_mul_f32_e32 v162, 0x3dd53b94, v162
	v_exp_f32_e32 v162, v162
	v_mfma_f32_32x32x16_bf16 v[32:47], v[132:135], v[236:239], v[32:47]
	ds_read_b64_tr_b16 v[236:237], v167 offset:0x1400
	ds_read_b64_tr_b16 v[238:239], v167 offset:0x1c00
	ds_read_b64_tr_b16 v[240:241], v167 offset:0x2400
	ds_read_b64_tr_b16 v[242:243], v167 offset:0x2c00
	v_cmp_ge_f32_e32 vcc, s46, v161
	s_cmp_eq_u64 vcc, exec
	s_cselect_b64 s[6:7], -1, 0
	v_cndmask_b32_e64 v206, v162, 1.0, s[6:7]
	v_cndmask_b32_e64 v160, v160, v198, s[6:7]
	v_mul_f32_e32 v205, 0xbdd53b94, v160
	v_cmp_gt_f32_e32 vcc, 1.0, v206
	v_mfma_f32_32x32x16_bf16 v[32:47], v[136:139], v[244:247], v[32:47]
	ds_read_b64_tr_b16 v[244:245], v167 offset:0x3400
	ds_read_b64_tr_b16 v[246:247], v167 offset:0x3c00
	v_fmamk_f32 v87, v87, 0x3dd53b94, v205
	v_fmamk_f32 v80, v80, 0x3dd53b94, v205
	v_fmamk_f32 v81, v81, 0x3dd53b94, v205
	v_fmamk_f32 v82, v82, 0x3dd53b94, v205
	v_fmamk_f32 v83, v83, 0x3dd53b94, v205
	v_mfma_f32_32x32x16_bf16 v[32:47], v[208:211], v[248:251], v[32:47]
	v_fmamk_f32 v84, v84, 0x3dd53b94, v205
	v_fmamk_f32 v85, v85, 0x3dd53b94, v205
	v_fmamk_f32 v86, v86, 0x3dd53b94, v205
	v_fmamk_f32 v88, v88, 0x3dd53b94, v205
	v_fmamk_f32 v89, v89, 0x3dd53b94, v205
	s_waitcnt lgkmcnt(0)
	v_mfma_f32_32x32x16_bf16 v[16:31], v[128:131], v[232:235], v[16:31]
	ds_read_b64_tr_b16 v[232:233], v167 offset:0x600
	ds_read_b64_tr_b16 v[234:235], v167 offset:0xe00
	v_fmamk_f32 v90, v90, 0x3dd53b94, v205
	v_fmamk_f32 v91, v91, 0x3dd53b94, v205
	v_fmamk_f32 v92, v92, 0x3dd53b94, v205
	v_fmamk_f32 v93, v93, 0x3dd53b94, v205
	v_fmamk_f32 v94, v94, 0x3dd53b94, v205
	v_mfma_f32_32x32x16_bf16 v[16:31], v[132:135], v[236:239], v[16:31]
	ds_read_b64_tr_b16 v[236:237], v167 offset:0x1600
	ds_read_b64_tr_b16 v[238:239], v167 offset:0x1e00
	v_fmamk_f32 v95, v95, 0x3dd53b94, v205
	v_fmamk_f32 v215, v64, 0x3dd53b94, v205
	v_fmamk_f32 v216, v65, 0x3dd53b94, v205
	v_fmamk_f32 v217, v66, 0x3dd53b94, v205
	v_fmamk_f32 v218, v67, 0x3dd53b94, v205
	v_mfma_f32_32x32x16_bf16 v[16:31], v[136:139], v[240:243], v[16:31]
	ds_read_b64_tr_b16 v[240:241], v167 offset:0x2600
	ds_read_b64_tr_b16 v[242:243], v167 offset:0x2e00
	ds_read_b64_tr_b16 v[248:249], v167 offset:0x3600
	ds_read_b64_tr_b16 v[250:251], v167 offset:0x3e00
	v_fmamk_f32 v219, v68, 0x3dd53b94, v205
	v_fmamk_f32 v212, v73, 0x3dd53b94, v205
	v_fmamk_f32 v213, v74, 0x3dd53b94, v205
	v_fmamk_f32 v214, v75, 0x3dd53b94, v205
	v_mfma_f32_32x32x16_bf16 v[16:31], v[208:211], v[244:247], v[16:31]
	v_fmamk_f32 v207, v76, 0x3dd53b94, v205
	v_fmamk_f32 v220, v77, 0x3dd53b94, v205
	v_fmamk_f32 v221, v78, 0x3dd53b94, v205
	s_waitcnt lgkmcnt(0)
	v_mfma_f32_32x32x16_bf16 v[48:63], v[128:131], v[232:235], v[48:63]
	v_exp_f32_e32 v128, v80
	v_exp_f32_e32 v129, v82
	v_exp_f32_e32 v130, v84
	v_exp_f32_e32 v131, v86
	v_mfma_f32_32x32x16_bf16 v[48:63], v[132:135], v[236:239], v[48:63]
	v_exp_f32_e32 v132, v88
	v_exp_f32_e32 v133, v90
	v_exp_f32_e32 v134, v92
	v_exp_f32_e32 v135, v94
	v_mfma_f32_32x32x16_bf16 v[48:63], v[136:139], v[240:243], v[48:63]
	v_exp_f32_e32 v139, v89
	v_exp_f32_e32 v138, v91
	v_exp_f32_e32 v137, v93
	v_exp_f32_e32 v136, v95
	v_mfma_f32_32x32x16_bf16 v[48:63], v[208:211], v[248:251], v[48:63]
	v_exp_f32_e32 v161, v87
	v_exp_f32_e32 v198, v81
	v_exp_f32_e32 v163, v83
	v_exp_f32_e32 v162, v85
	v_fmamk_f32 v208, v69, 0x3dd53b94, v205
	v_fmamk_f32 v209, v70, 0x3dd53b94, v205
	v_fmamk_f32 v210, v71, 0x3dd53b94, v205
	v_fmamk_f32 v211, v72, 0x3dd53b94, v205
	v_fmac_f32_e32 v205, 0x3dd53b94, v79
	s_cbranch_vccz .LBB0_2016
	s_and_saveexec_b64 s[10:11], s[4:5]
	ds_write_b32 v189, v206 offset:128
	s_or_b64 exec, exec, s[10:11]
	s_waitcnt lgkmcnt(0)
	v_add_u32_e32 v248, s12, v169
	ds_read_b128 v[232:235], v248 offset:224
	ds_read_b128 v[236:239], v248 offset:192
	ds_read_b128 v[240:243], v248 offset:160
	ds_read_b128 v[244:247], v248 offset:128
	s_waitcnt lgkmcnt(3)
	v_pk_mul_f32 v[12:13], v[12:13], v[232:233]
	s_waitcnt lgkmcnt(2)
	v_pk_mul_f32 v[8:9], v[8:9], v[236:237]
	s_waitcnt lgkmcnt(1)
	v_pk_mul_f32 v[4:5], v[4:5], v[240:241]
	v_pk_mul_f32 v[14:15], v[14:15], v[234:235]
	v_pk_mul_f32 v[10:11], v[10:11], v[238:239]
	v_pk_mul_f32 v[6:7], v[6:7], v[242:243]
	s_waitcnt lgkmcnt(0)
	v_pk_mul_f32 v[2:3], v[2:3], v[246:247]
	v_pk_mul_f32 v[0:1], v[0:1], v[244:245]
	v_pk_mul_f32 v[44:45], v[44:45], v[232:233]
	v_pk_mul_f32 v[40:41], v[40:41], v[236:237]
	v_pk_mul_f32 v[36:37], v[36:37], v[240:241]
	v_pk_mul_f32 v[46:47], v[46:47], v[234:235]
	v_pk_mul_f32 v[42:43], v[42:43], v[238:239]
	v_pk_mul_f32 v[38:39], v[38:39], v[242:243]
	v_pk_mul_f32 v[34:35], v[34:35], v[246:247]
	v_pk_mul_f32 v[32:33], v[32:33], v[244:245]
	v_pk_mul_f32 v[28:29], v[28:29], v[232:233]
	v_pk_mul_f32 v[24:25], v[24:25], v[236:237]
	v_pk_mul_f32 v[20:21], v[20:21], v[240:241]
	v_pk_mul_f32 v[30:31], v[30:31], v[234:235]
	v_pk_mul_f32 v[26:27], v[26:27], v[238:239]
	v_pk_mul_f32 v[22:23], v[22:23], v[242:243]
	v_pk_mul_f32 v[18:19], v[18:19], v[246:247]
	v_pk_mul_f32 v[16:17], v[16:17], v[244:245]
	v_pk_mul_f32 v[60:61], v[60:61], v[232:233]
	v_pk_mul_f32 v[56:57], v[56:57], v[236:237]
	v_pk_mul_f32 v[52:53], v[52:53], v[240:241]
	v_pk_mul_f32 v[62:63], v[62:63], v[234:235]
	v_pk_mul_f32 v[58:59], v[58:59], v[238:239]
	v_pk_mul_f32 v[54:55], v[54:55], v[242:243]
	v_pk_mul_f32 v[50:51], v[50:51], v[246:247]
	v_pk_mul_f32 v[48:49], v[48:49], v[244:245]
.LBB0_2016:
	s_waitcnt vmcnt(0) lgkmcnt(0)
	s_barrier
	s_add_i32 s80, s13, 64
	s_cmp_lt_u32 s8, 2
	s_cselect_b32 s80, s80, s14
	s_mul_i32 s81, s80, 0xc00
	s_add_i32 s85, s82, 0xc000
	s_mov_b32 m0, s85
	s_add_i32 s85, s82, 0x12000
	buffer_load_dwordx4 v154, s[72:75], s81 offen lds
	s_mov_b32 m0, s85
	s_add_i32 s85, s82, 0xe000
	buffer_load_dwordx4 v155, s[72:75], s81 offen lds
	s_mov_b32 m0, s85
	s_add_i32 s81, s81, 0x18000
	buffer_load_dwordx4 v154, s[72:75], s81 offen lds
	s_lshl_b32 s81, s84, 11
	s_add_i32 s85, s82, 0x0
	s_mov_b32 m0, s85
	s_add_i32 s85, s82, 0x2000
	buffer_load_dwordx4 v158, s[76:79], s81 offen lds
	s_mov_b32 m0, s85
	s_add_i32 s81, s81, 0x10000
	buffer_load_dwordx4 v158, s[76:79], s81 offen lds
	s_mov_b32 s83, s80
	ds_read_b128 v[64:67], v180 offset:32768
	ds_read_b128 v[68:71], v180 offset:40960
	ds_read_b128 v[222:225], v181 offset:32768
	ds_read_b128 v[226:229], v181 offset:40960
	ds_read_b128 v[230:233], v182 offset:32768
	ds_read_b128 v[234:237], v182 offset:40960
	ds_read_b128 v[238:241], v183 offset:32768
	ds_read_b128 v[242:245], v183 offset:40960
	v_exp_f32_e32 v164, v215
	v_add_f32_e32 v215, 0, v128
	v_add_f32_e32 v215, v198, v215
	v_add_f32_e32 v215, v129, v215
	v_add_f32_e32 v215, v163, v215
	v_add_f32_e32 v215, v130, v215
	v_add_f32_e32 v215, v162, v215
	v_add_f32_e32 v215, v131, v215
	v_add_f32_e32 v215, v161, v215
	v_add_f32_e32 v215, v132, v215
	v_add_f32_e32 v215, v139, v215
	v_add_f32_e32 v215, v133, v215
	v_add_f32_e32 v215, v138, v215
	v_add_f32_e32 v215, v134, v215
	v_exp_f32_e32 v165, v216
	v_add_f32_e32 v215, v137, v215
	s_waitcnt lgkmcnt(7)
	v_mfma_f32_32x32x16_bf16 v[80:95], v[64:67], v[124:127], 0
	s_waitcnt lgkmcnt(6)
	v_mfma_f32_32x32x16_bf16 v[64:79], v[68:71], v[124:127], 0
	s_waitcnt lgkmcnt(5)
	v_mfma_f32_32x32x16_bf16 v[80:95], v[222:225], v[120:123], v[80:95]
	v_exp_f32_e32 v217, v217
	v_add_f32_e32 v215, v135, v215
	v_exp_f32_e32 v218, v218
	v_add_f32_e32 v215, v136, v215
	v_exp_f32_e32 v219, v219
	v_add_f32_e32 v215, v164, v215
	v_exp_f32_e32 v208, v208
	s_waitcnt lgkmcnt(4)
	v_mfma_f32_32x32x16_bf16 v[64:79], v[226:229], v[120:123], v[64:79]
	ds_read_b128 v[222:225], v184 offset:32768
	ds_read_b128 v[226:229], v184 offset:40960
	v_add_f32_e32 v215, v165, v215
	v_exp_f32_e32 v209, v209
	v_add_f32_e32 v215, v217, v215
	v_exp_f32_e32 v210, v210
	v_add_f32_e32 v215, v218, v215
	v_exp_f32_e32 v211, v211
	s_waitcnt lgkmcnt(5)
	v_mfma_f32_32x32x16_bf16 v[80:95], v[230:233], v[116:119], v[80:95]
	v_add_f32_e32 v215, v219, v215
	v_exp_f32_e32 v212, v212
	v_add_f32_e32 v215, v208, v215
	v_exp_f32_e32 v213, v213
	v_add_f32_e32 v215, v209, v215
	v_exp_f32_e32 v214, v214
	v_add_f32_e32 v215, v210, v215
	s_waitcnt lgkmcnt(4)
	v_mfma_f32_32x32x16_bf16 v[64:79], v[234:237], v[116:119], v[64:79]
	ds_read_b128 v[230:233], v185 offset:32768
	ds_read_b128 v[234:237], v185 offset:40960
	v_exp_f32_e32 v207, v207
	v_add_f32_e32 v215, v211, v215
	v_exp_f32_e32 v220, v220
	v_add_f32_e32 v215, v212, v215
	v_exp_f32_e32 v221, v221
	v_add_f32_e32 v215, v213, v215
	s_waitcnt lgkmcnt(5)
	v_mfma_f32_32x32x16_bf16 v[80:95], v[238:241], v[112:115], v[80:95]
	v_exp_f32_e32 v205, v205
	v_add_f32_e32 v215, v214, v215
	v_add_f32_e32 v215, v207, v215
	v_add_f32_e32 v215, v220, v215
	v_add_f32_e32 v215, v221, v215
	v_add_f32_e32 v215, v205, v215
	v_mov_b32_e32 v216, v215
	s_waitcnt lgkmcnt(4)
	v_mfma_f32_32x32x16_bf16 v[64:79], v[242:245], v[112:115], v[64:79]
	ds_read_b128 v[238:241], v186 offset:32768
	ds_read_b128 v[242:245], v186 offset:40960
	v_permlane32_swap_b32_e32 v215, v216
	v_cvt_pk_bf16_f32 v128, v128, v198
	v_cvt_pk_bf16_f32 v129, v129, v163
	v_cvt_pk_bf16_f32 v130, v130, v162
	v_cvt_pk_bf16_f32 v131, v131, v161
	s_waitcnt lgkmcnt(5)
	v_mfma_f32_32x32x16_bf16 v[80:95], v[222:225], v[108:111], v[80:95]
	v_cvt_pk_bf16_f32 v132, v132, v139
	v_cvt_pk_bf16_f32 v133, v133, v138
	v_cvt_pk_bf16_f32 v134, v134, v137
	v_cvt_pk_bf16_f32 v135, v135, v136
	v_cvt_pk_bf16_f32 v136, v164, v165
	v_cvt_pk_bf16_f32 v137, v217, v218
	v_cvt_pk_bf16_f32 v138, v219, v208
	s_waitcnt lgkmcnt(4)
	v_mfma_f32_32x32x16_bf16 v[64:79], v[226:229], v[108:111], v[64:79]
	ds_read_b128 v[222:225], v187 offset:32768
	ds_read_b128 v[226:229], v187 offset:40960
	v_cvt_pk_bf16_f32 v139, v209, v210
	v_cvt_pk_bf16_f32 v208, v211, v212
	v_cvt_pk_bf16_f32 v209, v213, v214
	v_cvt_pk_bf16_f32 v210, v207, v220
	v_cvt_pk_bf16_f32 v211, v221, v205
	v_permlane32_swap_b32_e32 v128, v130
	s_waitcnt lgkmcnt(5)
	v_mfma_f32_32x32x16_bf16 v[80:95], v[230:233], v[104:107], v[80:95]
	v_permlane32_swap_b32_e32 v129, v131
	v_permlane32_swap_b32_e32 v132, v134
	v_permlane32_swap_b32_e32 v133, v135
	v_permlane32_swap_b32_e32 v136, v138
	s_waitcnt lgkmcnt(4)
	v_mfma_f32_32x32x16_bf16 v[64:79], v[234:237], v[104:107], v[64:79]
	ds_read_b128 v[230:233], v191
	ds_read_b128 v[234:237], v191 offset:4096
	ds_read_b128 v[246:249], v190
	v_permlane32_swap_b32_e32 v137, v139
	v_permlane32_swap_b32_e32 v208, v210
	v_permlane32_swap_b32_e32 v209, v211
	s_waitcnt lgkmcnt(6)
	v_mfma_f32_32x32x16_bf16 v[80:95], v[238:241], v[100:103], v[80:95]
	s_waitcnt lgkmcnt(5)
	v_mfma_f32_32x32x16_bf16 v[64:79], v[242:245], v[100:103], v[64:79]
	ds_read_b128 v[238:241], v192
	ds_read_b128 v[242:245], v192 offset:4096
	ds_read_b128 v[250:253], v190 offset:1024
	s_waitcnt lgkmcnt(7)
	v_mfma_f32_32x32x16_bf16 v[80:95], v[222:225], v[96:99], v[80:95]
	s_waitcnt lgkmcnt(6)
	v_mfma_f32_32x32x16_bf16 v[64:79], v[226:229], v[96:99], v[64:79]
	ds_read_b128 v[222:225], v193
	ds_read_b128 v[226:229], v193 offset:4096
	s_waitcnt lgkmcnt(5)
	v_mfma_f32_32x32x16_bf16 v[80:95], v[230:233], v[246:249], v[80:95]
	s_waitcnt lgkmcnt(5)
	v_mfma_f32_32x32x16_bf16 v[64:79], v[234:237], v[246:249], v[64:79]
	ds_read_b128 v[230:233], v194
	ds_read_b128 v[234:237], v194 offset:4096
	ds_read_b128 v[246:249], v190 offset:2048
	s_waitcnt lgkmcnt(5)
	v_mfma_f32_32x32x16_bf16 v[80:95], v[238:241], v[250:253], v[80:95]
	s_waitcnt lgkmcnt(5)
	v_mfma_f32_32x32x16_bf16 v[64:79], v[242:245], v[250:253], v[64:79]
	ds_read_b128 v[250:253], v190 offset:3072
	s_waitcnt lgkmcnt(1)
	v_mfma_f32_32x32x16_bf16 v[80:95], v[222:225], v[246:249], v[80:95]
	s_waitcnt lgkmcnt(1)
	v_mfma_f32_32x32x16_bf16 v[64:79], v[226:229], v[246:249], v[64:79]
	s_waitcnt lgkmcnt(0)
	v_mfma_f32_32x32x16_bf16 v[80:95], v[230:233], v[250:253], v[80:95]
	s_waitcnt lgkmcnt(0)
	v_mfma_f32_32x32x16_bf16 v[64:79], v[234:237], v[250:253], v[64:79]
	ds_read_b64_tr_b16 v[238:239], v174 offset:0
	ds_read_b64_tr_b16 v[240:241], v174 offset:0x800
	ds_read_b64_tr_b16 v[242:243], v174 offset:0x1000
	ds_read_b64_tr_b16 v[244:245], v174 offset:0x1800
	ds_read_b64_tr_b16 v[246:247], v174 offset:0x2000
	ds_read_b64_tr_b16 v[248:249], v174 offset:0x2800
	ds_read_b64_tr_b16 v[250:251], v174 offset:0x3000
	ds_read_b64_tr_b16 v[252:253], v174 offset:0x3800
	s_nop 3
	v_max_f32_e32 v161, v81, v81
	v_max_f32_e32 v162, v80, v80
	v_max_f32_e32 v161, v162, v161
	v_max3_f32 v161, v161, v82, v83
	v_max3_f32 v161, v161, v84, v85
	v_max3_f32 v161, v161, v86, v87
	v_max3_f32 v161, v161, v88, v89
	v_max3_f32 v161, v161, v90, v91
	v_max3_f32 v161, v161, v92, v93
	v_max3_f32 v161, v161, v94, v95
	s_waitcnt lgkmcnt(0)
	v_mfma_f32_32x32x16_bf16 v[0:15], v[128:131], v[238:241], v[0:15]
	ds_read_b64_tr_b16 v[238:239], v174 offset:0x200
	ds_read_b64_tr_b16 v[240:241], v174 offset:0xa00
	v_max3_f32 v161, v161, v64, v65
	v_max3_f32 v161, v161, v66, v67
	v_max3_f32 v161, v161, v68, v69
	v_mfma_f32_32x32x16_bf16 v[0:15], v[132:135], v[242:245], v[0:15]
	ds_read_b64_tr_b16 v[242:243], v174 offset:0x1200
	ds_read_b64_tr_b16 v[244:245], v174 offset:0x1a00
	v_max3_f32 v161, v161, v70, v71
	v_max3_f32 v161, v161, v72, v73
	v_max3_f32 v161, v161, v74, v75
	v_mfma_f32_32x32x16_bf16 v[0:15], v[136:139], v[246:249], v[0:15]
	ds_read_b64_tr_b16 v[246:247], v174 offset:0x2200
	ds_read_b64_tr_b16 v[248:249], v174 offset:0x2a00
	ds_read_b64_tr_b16 v[162:163], v174 offset:0x3200
	ds_read_b64_tr_b16 v[164:165], v174 offset:0x3a00
	v_max3_f32 v161, v161, v76, v77
	v_max3_f32 v161, v161, v78, v79
	v_mov_b32_e32 v198, v161
	v_mfma_f32_32x32x16_bf16 v[0:15], v[208:211], v[250:253], v[0:15]
	v_max_f32_e32 v205, v160, v160
	v_permlane32_swap_b32_e32 v161, v198
	v_max_f32_e32 v198, v198, v198
	v_max_f32_e32 v161, v161, v161
	v_max_f32_e32 v161, v161, v198
	s_waitcnt lgkmcnt(0)
	v_mfma_f32_32x32x16_bf16 v[32:47], v[128:131], v[238:241], v[32:47]
	ds_read_b64_tr_b16 v[238:239], v174 offset:0x400
	ds_read_b64_tr_b16 v[240:241], v174 offset:0xc00
	v_sub_f32_e32 v198, v161, v160
	v_max_f32_e32 v161, v205, v161
	v_sub_f32_e32 v205, v160, v161
	v_mul_f32_e32 v205, 0x3dd53b94, v205
	v_exp_f32_e32 v205, v205
	v_mfma_f32_32x32x16_bf16 v[32:47], v[132:135], v[242:245], v[32:47]
	ds_read_b64_tr_b16 v[242:243], v174 offset:0x1400
	ds_read_b64_tr_b16 v[244:245], v174 offset:0x1c00
	v_cmp_ge_f32_e32 vcc, s46, v198
	s_cmp_eq_u64 vcc, exec
	s_cselect_b64 s[6:7], -1, 0
	v_cndmask_b32_e64 v205, v205, 1.0, s[6:7]
	v_cndmask_b32_e64 v198, v161, v160, s[6:7]
	v_mul_f32_e32 v236, 0xbdd53b94, v198
	v_mov_b32_e32 v237, v236
	v_cmp_gt_f32_e32 vcc, 1.0, v205
	v_mfma_f32_32x32x16_bf16 v[32:47], v[136:139], v[246:249], v[32:47]
	ds_read_b64_tr_b16 v[246:247], v174 offset:0x2400
	ds_read_b64_tr_b16 v[248:249], v174 offset:0x2c00
	ds_read_b64_tr_b16 v[250:251], v174 offset:0x3400
	ds_read_b64_tr_b16 v[252:253], v174 offset:0x3c00
	v_fmamk_f32 v80, v80, 0x3dd53b94, v236
	v_fmamk_f32 v81, v81, 0x3dd53b94, v236
	v_fmamk_f32 v82, v82, 0x3dd53b94, v236
	v_fmamk_f32 v83, v83, 0x3dd53b94, v236
	v_mfma_f32_32x32x16_bf16 v[32:47], v[208:211], v[162:165], v[32:47]
	v_fmamk_f32 v84, v84, 0x3dd53b94, v236
	v_fmamk_f32 v85, v85, 0x3dd53b94, v236
	v_fmamk_f32 v86, v86, 0x3dd53b94, v236
	v_fmamk_f32 v87, v87, 0x3dd53b94, v236
	s_waitcnt lgkmcnt(0)
	v_mfma_f32_32x32x16_bf16 v[16:31], v[128:131], v[238:241], v[16:31]
	ds_read_b64_tr_b16 v[162:163], v174 offset:0x600
	ds_read_b64_tr_b16 v[164:165], v174 offset:0xe00
	ds_read_b64_tr_b16 v[238:239], v174 offset:0x1600
	ds_read_b64_tr_b16 v[240:241], v174 offset:0x1e00
	v_fmamk_f32 v88, v88, 0x3dd53b94, v236
	v_fmamk_f32 v89, v89, 0x3dd53b94, v236
	v_fmamk_f32 v90, v90, 0x3dd53b94, v236
	v_fmamk_f32 v91, v91, 0x3dd53b94, v236
	v_mfma_f32_32x32x16_bf16 v[16:31], v[132:135], v[242:245], v[16:31]
	ds_read_b64_tr_b16 v[242:243], v174 offset:0x2600
	ds_read_b64_tr_b16 v[244:245], v174 offset:0x2e00
	v_fmamk_f32 v92, v92, 0x3dd53b94, v236
	v_fmamk_f32 v93, v93, 0x3dd53b94, v236
	v_fmamk_f32 v94, v94, 0x3dd53b94, v236
	v_fmamk_f32 v95, v95, 0x3dd53b94, v236
	v_mfma_f32_32x32x16_bf16 v[16:31], v[136:139], v[246:249], v[16:31]
	ds_read_b64_tr_b16 v[246:247], v174 offset:0x3600
	ds_read_b64_tr_b16 v[248:249], v174 offset:0x3e00
	v_exp_f32_e32 v222, v80
	v_exp_f32_e32 v224, v81
	v_exp_f32_e32 v220, v82
	v_mfma_f32_32x32x16_bf16 v[16:31], v[208:211], v[250:253], v[16:31]
	v_exp_f32_e32 v223, v83
	v_exp_f32_e32 v219, v84
	v_exp_f32_e32 v221, v85
	s_waitcnt lgkmcnt(0)
	v_mfma_f32_32x32x16_bf16 v[48:63], v[128:131], v[162:165], v[48:63]
	v_exp_f32_e32 v217, v86
	v_exp_f32_e32 v218, v87
	v_exp_f32_e32 v212, v88
	v_pk_fma_f32 v[130:131], v[70:71], s[26:27], v[236:237] op_sel_hi:[1,0,0]
	v_pk_fma_f32 v[128:129], v[72:73], s[26:27], v[236:237] op_sel_hi:[1,0,0]
	v_mfma_f32_32x32x16_bf16 v[48:63], v[132:135], v[238:241], v[48:63]
	v_exp_f32_e32 v214, v89
	v_exp_f32_e32 v213, v91
	v_exp_f32_e32 v207, v94
	v_pk_fma_f32 v[132:133], v[68:69], s[26:27], v[236:237] op_sel_hi:[1,0,0]
	v_pk_fma_f32 v[134:135], v[78:79], s[26:27], v[236:237] op_sel_hi:[1,0,0]
	v_mfma_f32_32x32x16_bf16 v[48:63], v[136:139], v[242:245], v[48:63]
	v_pk_fma_f32 v[138:139], v[64:65], s[26:27], v[236:237] op_sel_hi:[1,0,0]
	v_pk_fma_f32 v[136:137], v[66:67], s[26:27], v[236:237] op_sel_hi:[1,0,0]
	v_pk_fma_f32 v[162:163], v[74:75], s[26:27], v[236:237] op_sel_hi:[1,0,0]
	v_pk_fma_f32 v[160:161], v[76:77], s[26:27], v[236:237] op_sel_hi:[1,0,0]
	v_mfma_f32_32x32x16_bf16 v[48:63], v[208:211], v[246:249], v[48:63]
	v_exp_f32_e32 v211, v90
	v_exp_f32_e32 v208, v92
	v_exp_f32_e32 v210, v93
	v_exp_f32_e32 v209, v95
	v_add_f32_e32 v64, v203, v204
	v_fmac_f32_e32 v64, v197, v140
	v_add_f32_e32 v140, v215, v216
	s_addk_i32 s13, 0x80
	s_addk_i32 s14, 0x80
	v_fmac_f32_e32 v140, v64, v206
	s_cbranch_vccz .LBB0_2020
	s_and_saveexec_b64 s[10:11], s[4:5]
	ds_write_b32 v189, v205 offset:128
	s_or_b64 exec, exec, s[10:11]
	s_waitcnt lgkmcnt(0)
	v_add_u32_e32 v164, s12, v169
	ds_read_b128 v[238:241], v164 offset:224
	ds_read_b128 v[242:245], v164 offset:192
	ds_read_b128 v[246:249], v164 offset:160
	ds_read_b128 v[250:253], v164 offset:128
	s_waitcnt lgkmcnt(3)
	v_pk_mul_f32 v[12:13], v[12:13], v[238:239]
	s_waitcnt lgkmcnt(2)
	v_pk_mul_f32 v[8:9], v[8:9], v[242:243]
	s_waitcnt lgkmcnt(1)
	v_pk_mul_f32 v[4:5], v[4:5], v[246:247]
	v_pk_mul_f32 v[14:15], v[14:15], v[240:241]
	v_pk_mul_f32 v[10:11], v[10:11], v[244:245]
	v_pk_mul_f32 v[6:7], v[6:7], v[248:249]
	s_waitcnt lgkmcnt(0)
	v_pk_mul_f32 v[2:3], v[2:3], v[252:253]
	v_pk_mul_f32 v[0:1], v[0:1], v[250:251]
	v_pk_mul_f32 v[44:45], v[44:45], v[238:239]
	v_pk_mul_f32 v[40:41], v[40:41], v[242:243]
	v_pk_mul_f32 v[36:37], v[36:37], v[246:247]
	v_pk_mul_f32 v[46:47], v[46:47], v[240:241]
	v_pk_mul_f32 v[42:43], v[42:43], v[244:245]
	v_pk_mul_f32 v[38:39], v[38:39], v[248:249]
	v_pk_mul_f32 v[34:35], v[34:35], v[252:253]
	v_pk_mul_f32 v[32:33], v[32:33], v[250:251]
	v_pk_mul_f32 v[28:29], v[28:29], v[238:239]
	v_pk_mul_f32 v[24:25], v[24:25], v[242:243]
	v_pk_mul_f32 v[20:21], v[20:21], v[246:247]
	v_pk_mul_f32 v[30:31], v[30:31], v[240:241]
	v_pk_mul_f32 v[26:27], v[26:27], v[244:245]
	v_pk_mul_f32 v[22:23], v[22:23], v[248:249]
	v_pk_mul_f32 v[18:19], v[18:19], v[252:253]
	v_pk_mul_f32 v[16:17], v[16:17], v[250:251]
	v_pk_mul_f32 v[60:61], v[60:61], v[238:239]
	v_pk_mul_f32 v[56:57], v[56:57], v[242:243]
	v_pk_mul_f32 v[52:53], v[52:53], v[246:247]
	v_pk_mul_f32 v[62:63], v[62:63], v[240:241]
	v_pk_mul_f32 v[58:59], v[58:59], v[244:245]
	v_pk_mul_f32 v[54:55], v[54:55], v[248:249]
	v_pk_mul_f32 v[50:51], v[50:51], v[252:253]
	v_pk_mul_f32 v[48:49], v[48:49], v[250:251]
